# index_scores: query fragments of all 16 heads staged through LDS with coalesced loads; the 16 scattered per-wave global loads for heads 0-7 removed
# speedup vs baseline: 1.0217x; 1.0055x over previous
.LBB0_437:
	s_and_b64 s[6:7], s[4:5], exec
	s_cselect_b32 s18, s16, s17
	s_lshl_b32 s6, s18, 4
	s_add_i32 s20, s6, s19
	s_waitcnt vmcnt(15)
	v_add_u32_e32 v2, s20, v90
	v_mov_b64_e32 v[0:1], s[12:13]
	v_mad_i64_i32 v[2:3], s[6:7], v2, s96, v[0:1]
	v_lshl_add_u64 v[2:3], v[2:3], 0, v[32:33]
	s_waitcnt vmcnt(14)
	v_add_u32_e32 v4, s20, v91
	v_add_co_u32_e32 v2, vcc, s75, v2
	v_mad_i64_i32 v[4:5], s[6:7], v4, s96, v[0:1]
	s_nop 0
	v_addc_co_u32_e32 v3, vcc, 0, v3, vcc
	v_lshl_add_u64 v[4:5], v[4:5], 0, v[32:33]
	v_add_co_u32_e32 v4, vcc, s75, v4
	v_or_b32_e32 v104, s20, v118
	s_nop 0
	v_addc_co_u32_e32 v5, vcc, 0, v5, vcc
	s_barrier
	v_lshrrev_b32_e32 v2, 7, v119
	v_and_b32_e32 v3, 0x7f, v119
	v_lshlrev_b32_e32 v3, 4, v3
	v_mul_u32_u24_e32 v92, 0x810, v2
	v_add_u32_e32 v92, v92, v3
	v_add_u32_e32 v2, s20, v2
	v_mul_u32_u24_e32 v2, s96, v2
	v_add_u32_e32 v2, v2, v3
	v_add_u32_e32 v2, 0x8800, v2
	global_load_dwordx4 v[96:99], v2, s[12:13]
	v_add_u32_e32 v3, 0x24000, v2
	global_load_dwordx4 v[100:103], v3, s[12:13]
	v_add_u32_e32 v3, 0x48000, v2
	global_load_dwordx4 v[208:211], v3, s[12:13]
	v_add_u32_e32 v3, 0x6c000, v2
	global_load_dwordx4 v[212:215], v3, s[12:13]
	v_mad_i64_i32 v[0:1], s[6:7], v104, s96, v[0:1]
	v_lshlrev_b32_e32 v4, 1, v86
	v_mov_b32_e32 v5, v33
	v_ashrrev_i32_e32 v105, 31, v104
	v_lshl_add_u64 v[0:1], v[0:1], 0, v[4:5]
	v_lshlrev_b64 v[2:3], 10, v[104:105]
	s_mov_b64 s[6:7], 0x8800
	s_waitcnt vmcnt(5)
	v_add_co_u32_e32 v62, vcc, s75, v0
	v_lshl_add_u64 v[2:3], s[14:15], 0, v[2:3]
	s_waitcnt vmcnt(4)
	v_lshl_add_u64 v[66:67], v[0:1], 0, s[6:7]
	v_addc_co_u32_e32 v63, vcc, 0, v1, vcc
	global_load_dwordx4 v[70:73], v[2:3], off offset:560
	global_load_dwordx4 v[74:77], v[2:3], off offset:544
	global_load_dwordx4 v[78:81], v[2:3], off offset:528
	global_load_dwordx4 v[82:85], v[2:3], off offset:512
	s_ashr_i32 s6, s18, 31
	s_lshr_b32 s6, s6, 30
	s_add_i32 s18, s18, s6
	s_and_b32 s7, s18, -4
	s_add_i32 s6, s7, 4
	v_lshl_or_b32 v95, v104, 13, v86
	s_cmp_ge_i32 s8, s6
	s_mov_b32 s18, -1
	s_waitcnt vmcnt(7)
	ds_write_b128 v92, v[96:99]
	s_waitcnt vmcnt(6)
	ds_write_b128 v92, v[100:103] offset:8256
	s_waitcnt vmcnt(5)
	ds_write_b128 v92, v[208:211] offset:16512
	s_waitcnt vmcnt(4)
	ds_write_b128 v92, v[212:215] offset:24768
	v_mul_u32_u24_e32 v94, 0x810, v118
	v_add_u32_e32 v94, v94, v87
	s_waitcnt lgkmcnt(0)
	s_barrier
	s_cbranch_scc1 .LBB0_443
	ds_read_b128 v[62:65], v94
	ds_read_b128 v[0:3], v94 offset:64
	ds_read_b128 v[4:7], v94 offset:128
	ds_read_b128 v[8:11], v94 offset:192
	ds_read_b128 v[12:15], v94 offset:256
	ds_read_b128 v[16:19], v94 offset:320
	ds_read_b128 v[20:23], v94 offset:384
	ds_read_b128 v[24:27], v94 offset:448
	ds_read_b128 v[28:31], v94 offset:512
	ds_read_b128 v[38:41], v94 offset:576
	ds_read_b128 v[42:45], v94 offset:640
	ds_read_b128 v[46:49], v94 offset:704
	ds_read_b128 v[50:53], v94 offset:768
	ds_read_b128 v[54:57], v94 offset:832
	ds_read_b128 v[58:61], v94 offset:896
	ds_read_b128 v[66:69], v94 offset:960
	s_waitcnt lgkmcnt(0)
	ds_read_b128 v[140:143], v94 offset:1024
	ds_read_b128 v[144:147], v94 offset:1088
	ds_read_b128 v[148:151], v94 offset:1152
	ds_read_b128 v[152:155], v94 offset:1216
	ds_read_b128 v[156:159], v94 offset:1280
	ds_read_b128 v[160:163], v94 offset:1344
	ds_read_b128 v[164:167], v94 offset:1408
	ds_read_b128 v[168:171], v94 offset:1472
	ds_read_b128 v[172:175], v94 offset:1536
	ds_read_b128 v[176:179], v94 offset:1600
	ds_read_b128 v[180:183], v94 offset:1664
	ds_read_b128 v[184:187], v94 offset:1728
	ds_read_b128 v[188:191], v94 offset:1792
	ds_read_b128 v[192:195], v94 offset:1856
	ds_read_b128 v[196:199], v94 offset:1920
	ds_read_b128 v[200:203], v94 offset:1984
	s_waitcnt vmcnt(3)
	v_mul_f32_e32 v100, 0.5, v70
	v_or_b32_e32 v70, s19, v118
	v_lshl_or_b32 v104, v70, 7, v87
	s_waitcnt vmcnt(0)
	v_mul_f32_e32 v82, 0.5, v82
	v_mul_f32_e32 v83, 0.5, v83
	v_mul_f32_e32 v84, 0.5, v84
	v_mul_f32_e32 v85, 0.5, v85
	v_mul_f32_e32 v78, 0.5, v78
	v_mul_f32_e32 v79, 0.5, v79
	v_mul_f32_e32 v80, 0.5, v80
	v_mul_f32_e32 v81, 0.5, v81
	v_mul_f32_e32 v96, 0.5, v74
	v_mul_f32_e32 v97, 0.5, v75
	v_mul_f32_e32 v98, 0.5, v76
	v_mul_f32_e32 v99, 0.5, v77
	v_mul_f32_e32 v101, 0.5, v71
	v_mul_f32_e32 v102, 0.5, v72
	v_mul_f32_e32 v103, 0.5, v73
	v_add_u32_e32 v107, s10, v104
	v_add_u32_e32 v106, s9, v104
	s_or_b32 s7, s7, 3
	v_or_b32_e32 v105, 64, v104
	s_mov_b32 s21, -1
	s_mov_b32 s20, s11
	s_mov_b32 s19, s8
	global_load_dwordx4 v[132:135], v107, s[2:3]
	global_load_dwordx4 v[136:139], v106, s[2:3]
	s_waitcnt lgkmcnt(0)
